# RG final pass output gating regenerated by hand: gelu_tanh(gr)*h with packed f32 ops (same operation order), two chains interleaved, -400 VALU instructions per unit
# speedup vs baseline: 1.0030x; 1.0030x over previous
.LBB0_621:
	v_add_u32_e32 v128, 0, v117
	v_add_u32_e32 v34, 0x1c200, v128
	v_add_u32_e32 v35, 0x1c300, v128
	v_add_u32_e32 v36, 0x1c400, v128
	v_add_u32_e32 v37, 0x1c500, v128
	v_add_u32_e32 v38, 0x1c600, v128
	v_add_u32_e32 v118, 0, v0
	ds_read_b32 v34, v34
	ds_read_b32 v35, v35
	ds_read_b32 v36, v36
	ds_read_b32 v37, v37
	ds_read_b32 v127, v38
	ds_read_u16 v38, v118
	ds_read_u16 v40, v118 offset:288
	ds_read_u16 v42, v118 offset:576
	ds_read_u16 v44, v118 offset:864
	ds_read_u16 v39, v118 offset:144
	ds_read_u16 v41, v118 offset:432
	ds_read_u16 v43, v118 offset:720
	v_add_u32_e32 v68, 0x1c700, v128
	ds_read_b32 v143, v68
	s_waitcnt lgkmcnt(7)
	v_lshlrev_b32_e32 v38, 16, v38
	v_add_u32_e32 v68, 0x1c900, v128
	v_fma_f32 v119, v34, v38, v127
	ds_read_u16 v38, v118 offset:2304
	ds_read_b32 v137, v68
	s_waitcnt lgkmcnt(5)
	v_lshlrev_b32_e32 v39, 16, v39
	v_lshlrev_b32_e32 v40, 16, v40
	v_fmac_f32_e32 v119, v35, v39
	v_fma_f32 v120, v34, v39, v127
	ds_read_u16 v39, v118 offset:2448
	s_waitcnt lgkmcnt(5)
	v_lshlrev_b32_e32 v41, 16, v41
	v_fmac_f32_e32 v119, v36, v40
	v_fmac_f32_e32 v120, v35, v40
	v_fma_f32 v121, v34, v40, v127
	ds_read_u16 v40, v118 offset:2592
	v_lshlrev_b32_e32 v42, 16, v42
	v_fmac_f32_e32 v119, v37, v41
	v_fmac_f32_e32 v120, v36, v41
	v_fmac_f32_e32 v121, v35, v41
	v_fma_f32 v122, v34, v41, v127
	ds_read_u16 v41, v118 offset:2736
	s_waitcnt lgkmcnt(6)
	v_lshlrev_b32_e32 v43, 16, v43
	v_fmac_f32_e32 v120, v37, v42
	v_fmac_f32_e32 v121, v36, v42
	v_fmac_f32_e32 v122, v35, v42
	ds_read_u16 v42, v118 offset:2880
	v_lshlrev_b32_e32 v44, 16, v44
	v_fmac_f32_e32 v121, v37, v43
	v_fmac_f32_e32 v122, v36, v43
	s_waitcnt lgkmcnt(5)
	v_lshlrev_b32_e32 v38, 16, v38
	ds_read_u16 v43, v118 offset:3024
	v_fmac_f32_e32 v122, v37, v44
	ds_read_u16 v44, v118 offset:3168
	v_fma_f32 v123, v34, v38, v127
	ds_read_u16 v38, v118 offset:4608
	s_waitcnt lgkmcnt(6)
	v_lshlrev_b32_e32 v39, 16, v39
	s_waitcnt lgkmcnt(5)
	v_lshlrev_b32_e32 v40, 16, v40
	v_fmac_f32_e32 v123, v35, v39
	v_fma_f32 v124, v34, v39, v127
	ds_read_u16 v39, v118 offset:4752
	s_waitcnt lgkmcnt(5)
	v_lshlrev_b32_e32 v41, 16, v41
	v_fmac_f32_e32 v123, v36, v40
	v_fmac_f32_e32 v124, v35, v40
	v_fma_f32 v125, v34, v40, v127
	ds_read_u16 v40, v118 offset:4896
	s_waitcnt lgkmcnt(5)
	v_lshlrev_b32_e32 v42, 16, v42
	v_fmac_f32_e32 v123, v37, v41
	v_fmac_f32_e32 v124, v36, v41
	v_fmac_f32_e32 v125, v35, v41
	v_fma_f32 v126, v34, v41, v127
	ds_read_u16 v41, v118 offset:5040
	s_waitcnt lgkmcnt(5)
	v_lshlrev_b32_e32 v43, 16, v43
	v_fmac_f32_e32 v124, v37, v42
	v_fmac_f32_e32 v125, v36, v42
	v_fmac_f32_e32 v126, v35, v42
	ds_read_u16 v42, v118 offset:5184
	s_waitcnt lgkmcnt(5)
	v_lshlrev_b32_e32 v44, 16, v44
	v_fmac_f32_e32 v125, v37, v43
	v_fmac_f32_e32 v126, v36, v43
	s_waitcnt lgkmcnt(4)
	v_lshlrev_b32_e32 v38, 16, v38
	ds_read_u16 v43, v118 offset:5328
	v_fmac_f32_e32 v126, v37, v44
	ds_read_u16 v44, v118 offset:5472
	v_fma_f32 v129, v34, v38, v127
	ds_read_u16 v38, v118 offset:6912
	s_waitcnt lgkmcnt(6)
	v_lshlrev_b32_e32 v39, 16, v39
	s_waitcnt lgkmcnt(5)
	v_lshlrev_b32_e32 v40, 16, v40
	v_fmac_f32_e32 v129, v35, v39
	v_fma_f32 v130, v34, v39, v127
	s_waitcnt lgkmcnt(4)
	v_lshlrev_b32_e32 v41, 16, v41
	v_fmac_f32_e32 v129, v36, v40
	v_fmac_f32_e32 v130, v35, v40
	v_fma_f32 v131, v34, v40, v127
	s_waitcnt lgkmcnt(3)
	v_lshlrev_b32_e32 v42, 16, v42
	v_fmac_f32_e32 v129, v37, v41
	v_fmac_f32_e32 v130, v36, v41
	v_fmac_f32_e32 v131, v35, v41
	v_fma_f32 v132, v34, v41, v127
	ds_read_u16 v39, v118 offset:7056
	ds_read_u16 v40, v118 offset:7200
	ds_read_u16 v41, v118 offset:7344
	s_waitcnt lgkmcnt(5)
	v_lshlrev_b32_e32 v43, 16, v43
	v_fmac_f32_e32 v130, v37, v42
	v_fmac_f32_e32 v131, v36, v42
	v_fmac_f32_e32 v132, v35, v42
	ds_read_u16 v42, v118 offset:7488
	s_waitcnt lgkmcnt(5)
	v_lshlrev_b32_e32 v44, 16, v44
	v_fmac_f32_e32 v131, v37, v43
	v_fmac_f32_e32 v132, v36, v43
	ds_read_u16 v43, v118 offset:7632
	v_fmac_f32_e32 v132, v37, v44
	ds_read_u16 v44, v118 offset:7776
	s_waitcnt lgkmcnt(6)
	v_lshlrev_b32_e32 v38, 16, v38
	s_waitcnt lgkmcnt(5)
	v_lshlrev_b32_e32 v39, 16, v39
	s_waitcnt lgkmcnt(4)
	v_lshlrev_b32_e32 v40, 16, v40
	s_waitcnt lgkmcnt(3)
	v_lshlrev_b32_e32 v41, 16, v41
	s_waitcnt lgkmcnt(2)
	v_lshlrev_b32_e32 v42, 16, v42
	v_fma_f32 v133, v34, v38, v127
	v_fma_f32 v134, v34, v39, v127
	v_fma_f32 v135, v34, v40, v127
	v_fmac_f32_e32 v127, v34, v41
	s_waitcnt lgkmcnt(1)
	v_lshlrev_b32_e32 v43, 16, v43
	v_fmac_f32_e32 v133, v35, v39
	v_fmac_f32_e32 v134, v35, v40
	v_fmac_f32_e32 v135, v35, v41
	v_fmac_f32_e32 v127, v35, v42
	v_add_u32_e32 v136, 0, v116
	s_waitcnt lgkmcnt(0)
	v_lshlrev_b32_e32 v44, 16, v44
	v_fmac_f32_e32 v133, v36, v40
	v_fmac_f32_e32 v134, v36, v41
	v_fmac_f32_e32 v135, v36, v42
	v_fmac_f32_e32 v127, v36, v43
	v_add_u32_e32 v34, 0x13200, v136
	v_fmac_f32_e32 v133, v37, v41
	v_fmac_f32_e32 v134, v37, v42
	v_fmac_f32_e32 v135, v37, v43
	v_fmac_f32_e32 v127, v37, v44
	ds_read_b128 v[34:37], v34
	v_add_u32_e32 v38, 0x13240, v136
	ds_read_b128 v[42:45], v38
	s_waitcnt lgkmcnt(1)
	v_mfma_f32_16x16x32_bf16 v[38:41], v[2:5], v[34:37], 0
	v_add_u32_e32 v50, 0x15640, v136
	ds_read_b128 v[138:141], v50
	v_add_u32_e32 v68, 0x1cb00, v128
	s_waitcnt lgkmcnt(1)
	v_mfma_f32_16x16x32_bf16 v[58:61], v[18:21], v[42:45], v[38:41]
	s_mov_b32 s13, 0x7b300000
	v_mfma_f32_16x16x32_bf16 v[38:41], v[6:9], v[34:37], 0
	v_mfma_f32_16x16x32_bf16 v[46:49], v[22:25], v[42:45], v[38:41]
	s_nop 4
	v_fmamk_f32 v58, v58, 0xbfb8aa3b, v143
	v_exp_f32_e32 v58, v58
	v_fmamk_f32 v59, v59, 0xbfb8aa3b, v143
	v_mfma_f32_16x16x32_bf16 v[38:41], v[10:13], v[34:37], 0
	v_exp_f32_e32 v59, v59
	v_add_f32_e32 v58, 1.0, v58
	v_rcp_f32_e64 v58, -v58
	v_mfma_f32_16x16x32_bf16 v[34:37], v[14:17], v[34:37], 0
	v_add_f32_e32 v59, 1.0, v59
	v_rcp_f32_e64 v59, -v59
	v_fmamk_f32 v60, v60, 0xbfb8aa3b, v143
	v_mfma_f32_16x16x32_bf16 v[38:41], v[26:29], v[42:45], v[38:41]
	v_exp_f32_e32 v60, v60
	v_fmamk_f32 v61, v61, 0xbfb8aa3b, v143
	v_exp_f32_e32 v61, v61
	v_mfma_f32_16x16x32_bf16 v[34:37], v[30:33], v[42:45], v[34:37]
	v_add_u32_e32 v42, 0x15600, v136
	ds_read_b128 v[42:45], v42
	v_add_f32_e32 v60, 1.0, v60
	s_waitcnt lgkmcnt(0)
	v_mfma_f32_16x16x32_bf16 v[50:53], v[2:5], v[42:45], 0
	v_rcp_f32_e64 v60, -v60
	v_add_f32_e32 v61, 1.0, v61
	v_rcp_f32_e64 v61, -v61
	v_mfma_f32_16x16x32_bf16 v[62:65], v[18:21], v[138:141], v[50:53]
	v_mfma_f32_16x16x32_bf16 v[50:53], v[6:9], v[42:45], 0
	v_mfma_f32_16x16x32_bf16 v[54:57], v[22:25], v[138:141], v[50:53]
	s_nop 5
	v_fmamk_f32 v62, v62, 0xbfb8aa3b, v137
	v_exp_f32_e32 v62, v62
	v_mfma_f32_16x16x32_bf16 v[50:53], v[10:13], v[42:45], 0
	v_add_f32_e32 v62, 1.0, v62
	v_rcp_f32_e32 v62, v62
	v_mfma_f32_16x16x32_bf16 v[42:45], v[14:17], v[42:45], 0
	v_mfma_f32_16x16x32_bf16 v[50:53], v[26:29], v[138:141], v[50:53]
	v_mfma_f32_16x16x32_bf16 v[42:45], v[30:33], v[138:141], v[42:45]
	ds_read_b32 v139, v68
	v_lshl_add_u64 v[68:69], v[66:67], 0, s[4:5]
	v_add_co_u32_e32 v140, vcc, s13, v68
	s_waitcnt lgkmcnt(0)
	v_mul_f32_e32 v58, v139, v58
	v_addc_co_u32_e32 v141, vcc, 0, v69, vcc
	s_waitcnt vmcnt(0)
	v_mov_b32_e32 v138, v194
	s_cmp_eq_u32 s4, 64
	s_cselect_b64 s[34:35], -1, 0
	v_cndmask_b32_e64 v138, v138, v195, s[34:35]
	s_cmp_eq_u32 s4, 0x80
	s_cselect_b64 s[34:35], -1, 0
	v_cndmask_b32_e64 v138, v138, v196, s[34:35]
	s_cmp_eq_u32 s4, 0xc0
	s_cselect_b64 s[34:35], -1, 0
	v_cndmask_b32_e64 v138, v138, v197, s[34:35]
	v_exp_f32_e32 v140, v58
	v_mul_f32_e32 v59, v139, v59
	v_exp_f32_e32 v59, v59
	v_mul_f32_e32 v60, v139, v60
	v_fma_f32 v58, -v140, v140, 1.0
	v_sqrt_f32_e32 v58, v58
	v_exp_f32_e32 v60, v60
	v_mul_f32_e32 v61, v139, v61
	v_exp_f32_e32 v61, v61
	v_mul_f32_e32 v58, v62, v58
	v_fmamk_f32 v62, v63, 0xbfb8aa3b, v137
	v_exp_f32_e32 v62, v62
	v_fma_f32 v63, -v59, v59, 1.0
	v_sqrt_f32_e32 v63, v63
	v_mul_f32_e32 v58, v119, v58
	v_add_f32_e32 v62, 1.0, v62
	v_rcp_f32_e32 v62, v62
	s_nop 0
	v_mul_f32_e32 v62, v62, v63
	v_fmamk_f32 v63, v64, 0xbfb8aa3b, v137
	v_exp_f32_e32 v63, v63
	v_fma_f32 v64, -v60, v60, 1.0
	v_sqrt_f32_e32 v64, v64
	v_add_f32_e32 v63, 1.0, v63
	v_rcp_f32_e32 v63, v63
	s_nop 0
	v_mul_f32_e32 v63, v63, v64
	v_fmamk_f32 v64, v65, 0xbfb8aa3b, v137
	v_exp_f32_e32 v64, v64
	v_fma_f32 v65, -v61, v61, 1.0
	v_sqrt_f32_e32 v65, v65
	v_add_f32_e32 v64, 1.0, v64
	v_rcp_f32_e32 v64, v64
	s_nop 0
	v_mul_f32_e32 v64, v64, v65
	v_mul_f32_e32 v65, v59, v140
	v_mul_f32_e32 v59, v59, v58
	v_fmac_f32_e32 v59, v120, v62
	v_mul_f32_e32 v141, v60, v65
	v_mul_f32_e32 v60, v60, v59
	v_fmac_f32_e32 v60, v121, v63
	v_mul_f32_e32 v142, v61, v141
	v_mul_f32_e32 v61, v61, v60
	v_fmac_f32_e32 v61, v122, v64
	ds_bpermute_b32 v62, v98, v142
	ds_bpermute_b32 v63, v98, v61
	ds_bpermute_b32 v64, v99, v142
	ds_bpermute_b32 v144, v99, v61
	ds_bpermute_b32 v145, v100, v142
	ds_bpermute_b32 v146, v100, v61
	ds_bpermute_b32 v147, v101, v142
	ds_bpermute_b32 v148, v101, v61
	s_waitcnt vmcnt(0) lgkmcnt(6)
	v_fmac_f32_e32 v63, v138, v62
	v_cndmask_b32_e64 v62, v138, v63, s[42:43]
	s_waitcnt lgkmcnt(4)
	v_fmac_f32_e32 v144, v63, v64
	v_cndmask_b32_e64 v62, v62, v144, s[44:45]
	s_waitcnt lgkmcnt(2)
	v_fmac_f32_e32 v146, v144, v145
	v_cndmask_b32_e64 v62, v62, v146, s[46:47]
	s_waitcnt lgkmcnt(0)
	v_fmac_f32_e32 v148, v146, v147
	v_fmac_f32_e32 v58, v140, v62
	v_fmac_f32_e32 v59, v65, v62
	v_fmac_f32_e32 v60, v141, v62
	v_fmac_f32_e32 v61, v142, v62
	v_fmamk_f32 v46, v46, 0xbfb8aa3b, v143
	v_exp_f32_e32 v46, v46
	v_fmamk_f32 v47, v47, 0xbfb8aa3b, v143
	v_exp_f32_e32 v47, v47
	v_fmamk_f32 v48, v48, 0xbfb8aa3b, v143
	v_add_f32_e32 v46, 1.0, v46
	v_rcp_f32_e64 v46, -v46
	v_exp_f32_e32 v48, v48
	v_fmamk_f32 v49, v49, 0xbfb8aa3b, v143
	v_exp_f32_e32 v49, v49
	v_fmamk_f32 v54, v54, 0xbfb8aa3b, v137
	v_mul_f32_e32 v46, v139, v46
	v_add_f32_e32 v47, 1.0, v47
	v_exp_f32_e32 v54, v54
	v_exp_f32_e32 v46, v46
	v_rcp_f32_e64 v47, -v47
	v_add_f32_e32 v48, 1.0, v48
	v_rcp_f32_e64 v48, -v48
	v_add_f32_e32 v49, 1.0, v49
	v_rcp_f32_e64 v49, -v49
	v_fmamk_f32 v55, v55, 0xbfb8aa3b, v137
	v_add_f32_e32 v54, 1.0, v54
	v_fma_f32 v62, -v46, v46, 1.0
	v_mul_f32_e32 v47, v139, v47
	v_rcp_f32_e32 v54, v54
	v_sqrt_f32_e32 v62, v62
	v_exp_f32_e32 v55, v55
	v_exp_f32_e32 v47, v47
	v_fmamk_f32 v56, v56, 0xbfb8aa3b, v137
	v_mul_f32_e32 v48, v139, v48
	v_exp_f32_e32 v56, v56
	v_exp_f32_e32 v48, v48
	v_fmamk_f32 v57, v57, 0xbfb8aa3b, v137
	v_mul_f32_e32 v49, v139, v49
	v_exp_f32_e32 v57, v57
	v_exp_f32_e32 v49, v49
	v_mul_f32_e32 v54, v54, v62
	v_add_f32_e32 v55, 1.0, v55
	v_fma_f32 v62, -v47, v47, 1.0
	v_rcp_f32_e32 v55, v55
	v_sqrt_f32_e32 v63, v62
	v_add_f32_e32 v56, 1.0, v56
	v_fma_f32 v62, -v48, v48, 1.0
	v_rcp_f32_e32 v56, v56
	v_sqrt_f32_e32 v64, v62
	v_add_f32_e32 v57, 1.0, v57
	v_fma_f32 v62, -v49, v49, 1.0
	v_rcp_f32_e32 v57, v57
	v_sqrt_f32_e32 v65, v62
	v_mul_f32_e32 v62, v123, v54
	v_mul_f32_e32 v54, v55, v63
	v_mul_f32_e32 v63, v47, v62
	v_fmac_f32_e32 v63, v124, v54
	v_mul_f32_e32 v55, v56, v64
	v_mul_f32_e32 v64, v48, v63
	v_mul_f32_e32 v56, v57, v65
	v_mul_f32_e32 v57, v47, v46
	v_fmac_f32_e32 v64, v125, v55
	v_mul_f32_e32 v138, v48, v57
	v_mul_f32_e32 v65, v49, v64
	v_mul_f32_e32 v140, v49, v138
	v_fmac_f32_e32 v65, v126, v56
	ds_bpermute_b32 v47, v98, v140
	ds_bpermute_b32 v48, v98, v65
	ds_bpermute_b32 v49, v99, v140
	ds_bpermute_b32 v54, v99, v65
	ds_bpermute_b32 v55, v100, v140
	ds_bpermute_b32 v56, v100, v65
	ds_bpermute_b32 v141, v101, v140
	ds_bpermute_b32 v144, v101, v65
	s_waitcnt lgkmcnt(6)
	v_fmac_f32_e32 v48, v148, v47
	v_cndmask_b32_e64 v47, v148, v48, s[42:43]
	s_waitcnt lgkmcnt(4)
	v_fmac_f32_e32 v54, v48, v49
	v_cndmask_b32_e64 v47, v47, v54, s[44:45]
	s_waitcnt lgkmcnt(2)
	v_fmac_f32_e32 v56, v54, v55
	v_cndmask_b32_e64 v47, v47, v56, s[46:47]
	s_waitcnt lgkmcnt(0)
	v_fmac_f32_e32 v144, v56, v141
	v_fmac_f32_e32 v62, v46, v47
	v_fmac_f32_e32 v63, v57, v47
	v_fmac_f32_e32 v64, v138, v47
	v_fmac_f32_e32 v65, v140, v47
	v_fmamk_f32 v38, v38, 0xbfb8aa3b, v143
	v_exp_f32_e32 v38, v38
	v_fmamk_f32 v39, v39, 0xbfb8aa3b, v143
	v_exp_f32_e32 v39, v39
	v_fmamk_f32 v40, v40, 0xbfb8aa3b, v143
	v_add_f32_e32 v38, 1.0, v38
	v_rcp_f32_e64 v38, -v38
	v_exp_f32_e32 v40, v40
	v_fmamk_f32 v41, v41, 0xbfb8aa3b, v143
	v_fmamk_f32 v46, v50, 0xbfb8aa3b, v137
	v_mul_f32_e32 v38, v139, v38
	v_add_f32_e32 v39, 1.0, v39
	v_exp_f32_e32 v41, v41
	v_exp_f32_e32 v46, v46
	v_exp_f32_e32 v38, v38
	v_rcp_f32_e64 v39, -v39
	v_add_f32_e32 v40, 1.0, v40
	v_rcp_f32_e64 v40, -v40
	v_add_f32_e32 v41, 1.0, v41
	v_fmamk_f32 v47, v51, 0xbfb8aa3b, v137
	v_add_f32_e32 v46, 1.0, v46
	v_fma_f32 v48, -v38, v38, 1.0
	v_mul_f32_e32 v39, v139, v39
	v_rcp_f32_e64 v41, -v41
	v_rcp_f32_e32 v46, v46
	v_sqrt_f32_e32 v48, v48
	v_exp_f32_e32 v47, v47
	v_exp_f32_e32 v39, v39
	v_fmamk_f32 v49, v52, 0xbfb8aa3b, v137
	v_mul_f32_e32 v40, v139, v40
	v_exp_f32_e32 v49, v49
	v_exp_f32_e32 v40, v40
	v_fmamk_f32 v51, v53, 0xbfb8aa3b, v137
	v_mul_f32_e32 v41, v139, v41
	v_mul_f32_e32 v46, v46, v48
	v_add_f32_e32 v47, 1.0, v47
	v_fma_f32 v48, -v39, v39, 1.0
	v_exp_f32_e32 v51, v51
	v_exp_f32_e32 v41, v41
	v_rcp_f32_e32 v47, v47
	v_sqrt_f32_e32 v48, v48
	v_add_f32_e32 v49, 1.0, v49
	v_fma_f32 v50, -v40, v40, 1.0
	v_rcp_f32_e32 v49, v49
	v_sqrt_f32_e32 v50, v50
	v_add_f32_e32 v51, 1.0, v51
	v_fma_f32 v52, -v41, v41, 1.0
	v_mul_f32_e32 v138, v129, v46
	v_rcp_f32_e32 v51, v51
	v_sqrt_f32_e32 v52, v52
	v_mul_f32_e32 v46, v47, v48
	v_mul_f32_e32 v140, v39, v138
	v_fmac_f32_e32 v140, v130, v46
	v_mul_f32_e32 v47, v49, v50
	v_mul_f32_e32 v141, v40, v140
	v_mul_f32_e32 v49, v39, v38
	v_fmac_f32_e32 v141, v131, v47
	v_mul_f32_e32 v48, v51, v52
	v_mul_f32_e32 v50, v40, v49
	v_mul_f32_e32 v142, v41, v141
	v_mul_f32_e32 v51, v41, v50
	v_fmac_f32_e32 v142, v132, v48
	ds_bpermute_b32 v39, v98, v51
	ds_bpermute_b32 v40, v98, v142
	ds_bpermute_b32 v41, v99, v51
	ds_bpermute_b32 v46, v99, v142
	ds_bpermute_b32 v47, v100, v51
	ds_bpermute_b32 v48, v100, v142
	ds_bpermute_b32 v52, v101, v51
	ds_bpermute_b32 v53, v101, v142
	s_waitcnt lgkmcnt(6)
	v_fmac_f32_e32 v40, v144, v39
	v_cndmask_b32_e64 v39, v144, v40, s[42:43]
	s_waitcnt lgkmcnt(4)
	v_fmac_f32_e32 v46, v40, v41
	v_cndmask_b32_e64 v39, v39, v46, s[44:45]
	s_waitcnt lgkmcnt(2)
	v_fmac_f32_e32 v48, v46, v47
	v_cndmask_b32_e64 v39, v39, v48, s[46:47]
	s_waitcnt lgkmcnt(0)
	v_fmac_f32_e32 v53, v48, v52
	v_fmac_f32_e32 v138, v38, v39
	v_fmac_f32_e32 v140, v49, v39
	v_fmac_f32_e32 v141, v50, v39
	v_fmac_f32_e32 v142, v51, v39
	v_fmamk_f32 v34, v34, 0xbfb8aa3b, v143
	v_exp_f32_e32 v34, v34
	v_fmamk_f32 v35, v35, 0xbfb8aa3b, v143
	v_exp_f32_e32 v35, v35
	v_fmamk_f32 v36, v36, 0xbfb8aa3b, v143
	v_add_f32_e32 v34, 1.0, v34
	v_rcp_f32_e64 v34, -v34
	v_exp_f32_e32 v36, v36
	v_fmac_f32_e32 v143, 0xbfb8aa3b, v37
	v_fmamk_f32 v38, v42, 0xbfb8aa3b, v137
	v_mul_f32_e32 v34, v139, v34
	v_add_f32_e32 v35, 1.0, v35
	v_exp_f32_e32 v37, v143
	v_exp_f32_e32 v38, v38
	v_exp_f32_e32 v34, v34
	v_rcp_f32_e64 v35, -v35
	v_add_f32_e32 v36, 1.0, v36
	v_rcp_f32_e64 v36, -v36
	v_add_f32_e32 v37, 1.0, v37
	v_fmamk_f32 v39, v43, 0xbfb8aa3b, v137
	v_add_f32_e32 v38, 1.0, v38
	v_fma_f32 v40, -v34, v34, 1.0
	v_mul_f32_e32 v35, v139, v35
	v_rcp_f32_e64 v37, -v37
	v_rcp_f32_e32 v38, v38
	v_sqrt_f32_e32 v40, v40
	v_exp_f32_e32 v39, v39
	v_exp_f32_e32 v35, v35
	v_fmamk_f32 v41, v44, 0xbfb8aa3b, v137
	v_mul_f32_e32 v36, v139, v36
	v_exp_f32_e32 v41, v41
	v_exp_f32_e32 v36, v36
	v_fmac_f32_e32 v137, 0xbfb8aa3b, v45
	v_mul_f32_e32 v37, v139, v37
	v_mul_f32_e32 v38, v38, v40
	v_add_f32_e32 v39, 1.0, v39
	v_fma_f32 v40, -v35, v35, 1.0
	v_exp_f32_e32 v43, v137
	v_exp_f32_e32 v37, v37
	v_rcp_f32_e32 v39, v39
	v_sqrt_f32_e32 v40, v40
	v_add_f32_e32 v41, 1.0, v41
	v_fma_f32 v42, -v36, v36, 1.0
	v_rcp_f32_e32 v41, v41
	v_sqrt_f32_e32 v42, v42
	v_add_f32_e32 v43, 1.0, v43
	v_fma_f32 v44, -v37, v37, 1.0
	v_mul_f32_e32 v139, v133, v38
	v_rcp_f32_e32 v43, v43
	v_sqrt_f32_e32 v44, v44
	v_mul_f32_e32 v38, v39, v40
	v_mul_f32_e32 v143, v35, v139
	v_fmac_f32_e32 v143, v134, v38
	v_mul_f32_e32 v39, v41, v42
	v_mul_f32_e32 v156, v36, v143
	v_mul_f32_e32 v41, v35, v34
	v_fmac_f32_e32 v156, v135, v39
	v_mul_f32_e32 v40, v43, v44
	v_mul_f32_e32 v42, v36, v41
	v_mul_f32_e32 v157, v37, v156
	v_mul_f32_e32 v43, v37, v42
	v_fmac_f32_e32 v157, v127, v40
	ds_bpermute_b32 v35, v98, v43
	ds_bpermute_b32 v36, v98, v157
	ds_bpermute_b32 v37, v99, v43
	ds_bpermute_b32 v38, v99, v157
	ds_bpermute_b32 v39, v100, v43
	ds_bpermute_b32 v40, v100, v157
	s_waitcnt lgkmcnt(4)
	v_fmac_f32_e32 v36, v53, v35
	v_cndmask_b32_e64 v35, v53, v36, s[42:43]
	s_waitcnt lgkmcnt(2)
	v_fmac_f32_e32 v38, v36, v37
	v_cndmask_b32_e64 v35, v35, v38, s[44:45]
	s_waitcnt lgkmcnt(0)
	v_fmac_f32_e32 v40, v38, v39
	v_cndmask_b32_e64 v35, v35, v40, s[46:47]
	v_fmac_f32_e32 v139, v34, v35
	v_fmac_f32_e32 v143, v41, v35
	v_fmac_f32_e32 v156, v42, v35
	v_fmac_f32_e32 v157, v43, v35
	s_mov_b32 s13, 0x7b720000
	v_add_co_u32_e32 v68, vcc, s13, v68
	v_add_u32_e32 v34, 0x17a00, v136
	v_add_u32_e32 v38, 0x17a40, v136
	v_add_u32_e32 v50, 0x19e00, v136
	v_add_u32_e32 v51, 0x19e40, v136
	v_add_u32_e32 v136, 0x1c800, v128
	v_addc_co_u32_e32 v69, vcc, 0, v69, vcc
	ds_read_b128 v[34:37], v34
	ds_read_b128 v[46:49], v38
	ds_read_b128 v[54:57], v50
	ds_read_b128 v[144:147], v51
	v_add_u32_e32 v152, 0x1ca00, v128
	v_add_u32_e32 v153, 0x1cc00, v128
	ds_read_b32 v137, v136
	ds_read_b32 v128, v152
	ds_read_b32 v136, v153
	s_waitcnt vmcnt(0)
	v_mov_b32_e32 v68, v198
	s_cmp_eq_u32 s4, 64
	s_cselect_b64 s[34:35], -1, 0
	v_cndmask_b32_e64 v68, v68, v199, s[34:35]
	s_cmp_eq_u32 s4, 0x80
	s_cselect_b64 s[34:35], -1, 0
	v_cndmask_b32_e64 v68, v68, v200, s[34:35]
	s_cmp_eq_u32 s4, 0xc0
	s_cselect_b64 s[34:35], -1, 0
	v_cndmask_b32_e64 v68, v68, v201, s[34:35]
	s_waitcnt lgkmcnt(6)
	v_mfma_f32_16x16x32_bf16 v[50:53], v[14:17], v[34:37], 0
	s_waitcnt lgkmcnt(5)
	v_mfma_f32_16x16x32_bf16 v[148:151], v[30:33], v[46:49], v[50:53]
	s_waitcnt lgkmcnt(4)
	v_mfma_f32_16x16x32_bf16 v[50:53], v[14:17], v[54:57], 0
	s_waitcnt lgkmcnt(3)
	v_mfma_f32_16x16x32_bf16 v[152:155], v[30:33], v[144:147], v[50:53]
	s_waitcnt lgkmcnt(2)
	s_nop 2
	v_fmamk_f32 v69, v148, 0xbfb8aa3b, v137
	v_fmamk_f32 v150, v150, 0xbfb8aa3b, v137
	v_exp_f32_e32 v150, v150
	v_exp_f32_e32 v50, v69
	v_mfma_f32_16x16x32_bf16 v[38:41], v[2:5], v[34:37], 0
	s_waitcnt lgkmcnt(1)
	v_fmamk_f32 v51, v152, 0xbfb8aa3b, v128
	v_exp_f32_e32 v51, v51
	v_add_f32_e32 v50, 1.0, v50
	v_rcp_f32_e64 v50, -v50
	v_mfma_f32_16x16x32_bf16 v[42:45], v[6:9], v[34:37], 0
	v_add_f32_e32 v51, 1.0, v51
	v_rcp_f32_e32 v69, v51
	s_waitcnt lgkmcnt(0)
	v_mul_f32_e32 v50, v136, v50
	v_mfma_f32_16x16x32_bf16 v[34:37], v[10:13], v[34:37], 0
	v_exp_f32_e32 v148, v50
	v_fmamk_f32 v154, v154, 0xbfb8aa3b, v128
	v_exp_f32_e32 v154, v154
	v_mfma_f32_16x16x32_bf16 v[50:53], v[26:29], v[46:49], v[34:37]
	v_mfma_f32_16x16x32_bf16 v[38:41], v[18:21], v[46:49], v[38:41]
	s_nop 2
	v_fmamk_f32 v34, v149, 0xbfb8aa3b, v137
	v_mfma_f32_16x16x32_bf16 v[42:45], v[22:25], v[46:49], v[42:45]
	v_exp_f32_e32 v46, v34
	v_fma_f32 v47, -v148, v148, 1.0
	v_sqrt_f32_e32 v149, v47
	v_fmamk_f32 v47, v153, 0xbfb8aa3b, v128
	v_add_f32_e32 v46, 1.0, v46
	v_rcp_f32_e64 v46, -v46
	v_mfma_f32_16x16x32_bf16 v[34:37], v[2:5], v[54:57], 0
	v_exp_f32_e32 v152, v47
	v_mul_f32_e32 v69, v69, v149
	v_mul_f32_e32 v153, v136, v46
	v_mfma_f32_16x16x32_bf16 v[46:49], v[6:9], v[54:57], 0
	v_exp_f32_e32 v153, v153
	v_add_f32_e32 v152, 1.0, v152
	v_rcp_f32_e32 v152, v152
	v_mfma_f32_16x16x32_bf16 v[54:57], v[10:13], v[54:57], 0
	v_fma_f32 v158, -v153, v153, 1.0
	v_sqrt_f32_e32 v158, v158
	v_mfma_f32_16x16x32_bf16 v[34:37], v[18:21], v[144:147], v[34:37]
	v_mul_f32_e32 v149, v152, v158
	v_mfma_f32_16x16x32_bf16 v[46:49], v[22:25], v[144:147], v[46:49]
	v_mfma_f32_16x16x32_bf16 v[54:57], v[26:29], v[144:147], v[54:57]
	v_fmamk_f32 v146, v151, 0xbfb8aa3b, v137
	v_exp_f32_e32 v146, v146
	v_add_f32_e32 v144, 1.0, v150
	v_rcp_f32_e64 v144, -v144
	v_fmamk_f32 v150, v155, 0xbfb8aa3b, v128
	v_add_f32_e32 v146, 1.0, v146
	v_rcp_f32_e64 v146, -v146
	v_mul_f32_e32 v144, v136, v144
	v_exp_f32_e32 v144, v144
	v_exp_f32_e32 v150, v150
	v_mul_f32_e32 v146, v136, v146
	v_exp_f32_e32 v146, v146
	v_add_f32_e32 v145, 1.0, v154
	v_fma_f32 v147, -v144, v144, 1.0
	v_add_f32_e32 v150, 1.0, v150
	v_fma_f32 v151, -v146, v146, 1.0
	v_rcp_f32_e32 v145, v145
	v_sqrt_f32_e32 v147, v147
	v_rcp_f32_e32 v150, v150
	v_sqrt_f32_e32 v151, v151
	v_mul_f32_e32 v145, v145, v147
	v_mul_f32_e32 v147, v150, v151
	v_mul_f32_e32 v147, v127, v147
	v_mul_f32_e32 v127, v144, v146
	v_mul_f32_e32 v144, v144, v147
	v_fmac_f32_e32 v144, v135, v145
	v_mul_f32_e32 v135, v153, v144
	v_fmac_f32_e32 v135, v134, v149
	v_mul_f32_e32 v150, v153, v127
	v_mul_f32_e32 v134, v148, v135
	v_mul_f32_e32 v151, v148, v150
	v_fmac_f32_e32 v134, v133, v69
	ds_bpermute_b32 v133, v101, v151
	ds_bpermute_b32 v148, v101, v134
	ds_bpermute_b32 v149, v100, v151
	ds_bpermute_b32 v152, v100, v134
	ds_bpermute_b32 v153, v99, v151
	ds_bpermute_b32 v154, v99, v134
	ds_bpermute_b32 v69, v98, v151
	ds_bpermute_b32 v145, v98, v134
	s_waitcnt vmcnt(0) lgkmcnt(6)
	v_fmac_f32_e32 v148, v68, v133
	v_cndmask_b32_e64 v68, v68, v148, s[44:45]
	s_waitcnt lgkmcnt(4)
	v_fmac_f32_e32 v152, v148, v149
	v_cndmask_b32_e64 v68, v68, v152, s[42:43]
	s_waitcnt lgkmcnt(2)
	v_fmac_f32_e32 v154, v152, v153
	v_cndmask_b32_e64 v133, v68, v154, s[40:41]
	v_fmac_f32_e32 v134, v151, v133
	v_fmac_f32_e32 v135, v150, v133
	v_fmac_f32_e32 v144, v127, v133
	v_fmac_f32_e32 v147, v146, v133
	s_waitcnt lgkmcnt(0)
	v_fmac_f32_e32 v145, v154, v69
	v_add_f32_e32 v68, v139, v134
	v_add_f32_e32 v69, v143, v135
	v_add_f32_e32 v127, v156, v144
	v_add_f32_e32 v133, v157, v147
	v_fmamk_f32 v50, v50, 0xbfb8aa3b, v137
	v_exp_f32_e32 v50, v50
	v_fmamk_f32 v51, v51, 0xbfb8aa3b, v137
	v_exp_f32_e32 v51, v51
	v_fmamk_f32 v54, v54, 0xbfb8aa3b, v128
	v_add_f32_e32 v50, 1.0, v50
	v_rcp_f32_e64 v50, -v50
	v_add_f32_e32 v51, 1.0, v51
	v_fmamk_f32 v52, v52, 0xbfb8aa3b, v137
	v_exp_f32_e32 v54, v54
	v_mul_f32_e32 v50, v136, v50
	v_exp_f32_e32 v50, v50
	v_rcp_f32_e64 v51, -v51
	v_exp_f32_e32 v52, v52
	v_add_f32_e32 v54, 1.0, v54
	v_fma_f32 v134, -v50, v50, 1.0
	v_fmamk_f32 v55, v55, 0xbfb8aa3b, v128
	v_mul_f32_e32 v51, v136, v51
	v_add_f32_e32 v52, 1.0, v52
	v_fmamk_f32 v53, v53, 0xbfb8aa3b, v137
	v_rcp_f32_e32 v54, v54
	v_sqrt_f32_e32 v134, v134
	v_exp_f32_e32 v55, v55
	v_exp_f32_e32 v51, v51
	v_rcp_f32_e64 v52, -v52
	v_exp_f32_e32 v53, v53
	v_mul_f32_e32 v54, v54, v134
	v_add_f32_e32 v55, 1.0, v55
	v_fma_f32 v134, -v51, v51, 1.0
	v_fmamk_f32 v56, v56, 0xbfb8aa3b, v128
	v_mul_f32_e32 v52, v136, v52
	v_add_f32_e32 v53, 1.0, v53
	v_rcp_f32_e32 v55, v55
	v_sqrt_f32_e32 v134, v134
	v_exp_f32_e32 v56, v56
	v_exp_f32_e32 v52, v52
	v_rcp_f32_e64 v53, -v53
	v_mul_f32_e32 v55, v55, v134
	v_add_f32_e32 v56, 1.0, v56
	v_fma_f32 v134, -v52, v52, 1.0
	v_fmamk_f32 v57, v57, 0xbfb8aa3b, v128
	v_mul_f32_e32 v53, v136, v53
	v_rcp_f32_e32 v56, v56
	v_sqrt_f32_e32 v134, v134
	v_exp_f32_e32 v57, v57
	v_exp_f32_e32 v53, v53
	v_mul_f32_e32 v56, v56, v134
	v_add_f32_e32 v57, 1.0, v57
	v_fma_f32 v134, -v53, v53, 1.0
	v_rcp_f32_e32 v57, v57
	v_sqrt_f32_e32 v134, v134
	s_nop 0
	v_mul_f32_e32 v57, v57, v134
	v_mul_f32_e32 v57, v132, v57
	v_mul_f32_e32 v132, v52, v53
	v_mul_f32_e32 v52, v52, v57
	v_fmac_f32_e32 v52, v131, v56
	v_mul_f32_e32 v134, v51, v132
	v_mul_f32_e32 v51, v51, v52
	v_fmac_f32_e32 v51, v130, v55
	v_mul_f32_e32 v135, v50, v134
	v_mul_f32_e32 v50, v50, v51
	v_fmac_f32_e32 v50, v129, v54
	ds_bpermute_b32 v139, v101, v135
	ds_bpermute_b32 v143, v101, v50
	ds_bpermute_b32 v130, v100, v135
	ds_bpermute_b32 v131, v100, v50
	ds_bpermute_b32 v56, v99, v135
	ds_bpermute_b32 v129, v99, v50
	ds_bpermute_b32 v54, v98, v135
	ds_bpermute_b32 v55, v98, v50
	s_waitcnt lgkmcnt(6)
	v_fmac_f32_e32 v143, v145, v139
	v_cndmask_b32_e64 v139, v145, v143, s[44:45]
	s_waitcnt lgkmcnt(4)
	v_fmac_f32_e32 v131, v143, v130
	v_cndmask_b32_e64 v130, v139, v131, s[42:43]
	s_waitcnt lgkmcnt(2)
	v_fmac_f32_e32 v129, v131, v56
	v_cndmask_b32_e64 v56, v130, v129, s[40:41]
	v_fmac_f32_e32 v50, v135, v56
	v_fmac_f32_e32 v51, v134, v56
	v_fmac_f32_e32 v52, v132, v56
	v_fmac_f32_e32 v57, v53, v56
	s_waitcnt lgkmcnt(0)
	v_fmac_f32_e32 v55, v129, v54
	v_add_f32_e32 v50, v138, v50
	v_add_f32_e32 v51, v140, v51
	v_add_f32_e32 v52, v141, v52
	v_add_f32_e32 v53, v142, v57
	v_fmamk_f32 v42, v42, 0xbfb8aa3b, v137
	v_exp_f32_e32 v42, v42
	v_fmamk_f32 v43, v43, 0xbfb8aa3b, v137
	v_exp_f32_e32 v43, v43
	v_fmamk_f32 v46, v46, 0xbfb8aa3b, v128
	v_add_f32_e32 v42, 1.0, v42
	v_rcp_f32_e64 v42, -v42
	v_add_f32_e32 v43, 1.0, v43
	v_fmamk_f32 v44, v44, 0xbfb8aa3b, v137
	v_exp_f32_e32 v46, v46
	v_mul_f32_e32 v42, v136, v42
	v_exp_f32_e32 v42, v42
	v_rcp_f32_e64 v43, -v43
	v_exp_f32_e32 v44, v44
	v_add_f32_e32 v46, 1.0, v46
	v_fma_f32 v54, -v42, v42, 1.0
	v_fmamk_f32 v47, v47, 0xbfb8aa3b, v128
	v_mul_f32_e32 v43, v136, v43
	v_add_f32_e32 v44, 1.0, v44
	v_fmamk_f32 v45, v45, 0xbfb8aa3b, v137
	v_rcp_f32_e32 v46, v46
	v_sqrt_f32_e32 v54, v54
	v_exp_f32_e32 v47, v47
	v_exp_f32_e32 v43, v43
	v_rcp_f32_e64 v44, -v44
	v_exp_f32_e32 v45, v45
	v_mul_f32_e32 v46, v46, v54
	v_add_f32_e32 v47, 1.0, v47
	v_fma_f32 v54, -v43, v43, 1.0
	v_fmamk_f32 v48, v48, 0xbfb8aa3b, v128
	v_mul_f32_e32 v44, v136, v44
	v_add_f32_e32 v45, 1.0, v45
	v_rcp_f32_e32 v47, v47
	v_sqrt_f32_e32 v54, v54
	v_exp_f32_e32 v48, v48
	v_exp_f32_e32 v44, v44
	v_rcp_f32_e64 v45, -v45
	v_mul_f32_e32 v47, v47, v54
	v_add_f32_e32 v48, 1.0, v48
	v_fma_f32 v54, -v44, v44, 1.0
	v_fmamk_f32 v49, v49, 0xbfb8aa3b, v128
	v_mul_f32_e32 v45, v136, v45
	v_rcp_f32_e32 v48, v48
	v_sqrt_f32_e32 v54, v54
	v_exp_f32_e32 v49, v49
	v_exp_f32_e32 v45, v45
	v_mul_f32_e32 v48, v48, v54
	v_add_f32_e32 v49, 1.0, v49
	v_fma_f32 v54, -v45, v45, 1.0
	v_rcp_f32_e32 v49, v49
	v_sqrt_f32_e32 v54, v54
	s_nop 0
	v_mul_f32_e32 v49, v49, v54
	v_mul_f32_e32 v49, v126, v49
	v_mul_f32_e32 v54, v44, v45
	v_mul_f32_e32 v44, v44, v49
	v_fmac_f32_e32 v44, v125, v48
	v_mul_f32_e32 v56, v43, v54
	v_mul_f32_e32 v43, v43, v44
	v_fmac_f32_e32 v43, v124, v47
	v_mul_f32_e32 v57, v42, v56
	v_mul_f32_e32 v42, v42, v43
	v_fmac_f32_e32 v42, v123, v46
	ds_bpermute_b32 v126, v101, v57
	ds_bpermute_b32 v129, v101, v42
	ds_bpermute_b32 v124, v100, v57
	ds_bpermute_b32 v125, v100, v42
	ds_bpermute_b32 v48, v99, v57
	ds_bpermute_b32 v123, v99, v42
	ds_bpermute_b32 v46, v98, v57
	ds_bpermute_b32 v47, v98, v42
	s_waitcnt lgkmcnt(6)
	v_fmac_f32_e32 v129, v55, v126
	v_cndmask_b32_e64 v55, v55, v129, s[44:45]
	s_waitcnt lgkmcnt(4)
	v_fmac_f32_e32 v125, v129, v124
	v_cndmask_b32_e64 v55, v55, v125, s[42:43]
	s_waitcnt lgkmcnt(2)
	v_fmac_f32_e32 v123, v125, v48
	v_cndmask_b32_e64 v48, v55, v123, s[40:41]
	v_fmac_f32_e32 v42, v57, v48
	v_fmac_f32_e32 v43, v56, v48
	v_fmac_f32_e32 v44, v54, v48
	v_fmac_f32_e32 v49, v45, v48
	s_waitcnt lgkmcnt(0)
	v_fmac_f32_e32 v47, v123, v46
	v_add_f32_e32 v42, v62, v42
	v_add_f32_e32 v43, v63, v43
	v_add_f32_e32 v44, v64, v44
	v_add_f32_e32 v45, v65, v49
	v_fmamk_f32 v38, v38, 0xbfb8aa3b, v137
	v_exp_f32_e32 v38, v38
	v_fmamk_f32 v39, v39, 0xbfb8aa3b, v137
	v_exp_f32_e32 v39, v39
	v_fmamk_f32 v40, v40, 0xbfb8aa3b, v137
	v_add_f32_e32 v38, 1.0, v38
	v_rcp_f32_e64 v38, -v38
	v_add_f32_e32 v39, 1.0, v39
	v_fmamk_f32 v34, v34, 0xbfb8aa3b, v128
	v_rcp_f32_e64 v39, -v39
	v_mul_f32_e32 v38, v136, v38
	v_exp_f32_e32 v38, v38
	v_exp_f32_e32 v40, v40
	v_exp_f32_e32 v34, v34
	v_mul_f32_e32 v39, v136, v39
	v_fmac_f32_e32 v137, 0xbfb8aa3b, v41
	v_add_f32_e32 v40, 1.0, v40
	v_add_f32_e32 v34, 1.0, v34
	v_fma_f32 v54, -v38, v38, 1.0
	v_fmamk_f32 v35, v35, 0xbfb8aa3b, v128
	v_exp_f32_e32 v39, v39
	v_rcp_f32_e64 v40, -v40
	v_exp_f32_e32 v41, v137
	v_rcp_f32_e32 v34, v34
	v_sqrt_f32_e32 v54, v54
	v_exp_f32_e32 v35, v35
	v_mul_f32_e32 v40, v136, v40
	v_add_f32_e32 v41, 1.0, v41
	v_mul_f32_e32 v34, v34, v54
	v_add_f32_e32 v35, 1.0, v35
	v_fma_f32 v54, -v39, v39, 1.0
	v_fmamk_f32 v36, v36, 0xbfb8aa3b, v128
	v_exp_f32_e32 v40, v40
	v_rcp_f32_e64 v41, -v41
	v_rcp_f32_e32 v35, v35
	v_sqrt_f32_e32 v54, v54
	v_exp_f32_e32 v36, v36
	v_mul_f32_e32 v41, v136, v41
	v_fmac_f32_e32 v128, 0xbfb8aa3b, v37
	v_mul_f32_e32 v35, v35, v54
	v_add_f32_e32 v36, 1.0, v36
	v_fma_f32 v54, -v40, v40, 1.0
	v_exp_f32_e32 v41, v41
	v_rcp_f32_e32 v36, v36
	v_sqrt_f32_e32 v54, v54
	v_exp_f32_e32 v37, v128
	v_mul_f32_e32 v46, v40, v41
	v_mul_f32_e32 v48, v39, v46
	v_mul_f32_e32 v36, v36, v54
	v_add_f32_e32 v37, 1.0, v37
	v_fma_f32 v54, -v41, v41, 1.0
	v_rcp_f32_e32 v37, v37
	v_sqrt_f32_e32 v54, v54
	v_mul_f32_e32 v49, v38, v48
	ds_bpermute_b32 v55, v101, v49
	v_mul_f32_e32 v37, v37, v54
	v_mul_f32_e32 v37, v122, v37
	v_mul_f32_e32 v40, v40, v37
	v_fmac_f32_e32 v40, v121, v36
	v_mul_f32_e32 v36, v39, v40
	v_fmac_f32_e32 v36, v120, v35
	v_mul_f32_e32 v35, v38, v36
	v_fmac_f32_e32 v35, v119, v34
	ds_bpermute_b32 v56, v101, v35
	ds_bpermute_b32 v39, v100, v49
	ds_bpermute_b32 v54, v100, v35
	ds_bpermute_b32 v34, v99, v49
	ds_bpermute_b32 v38, v99, v35
	s_waitcnt lgkmcnt(4)
	v_fmac_f32_e32 v56, v47, v55
	v_cndmask_b32_e64 v47, v47, v56, s[44:45]
	s_waitcnt lgkmcnt(2)
	v_fmac_f32_e32 v54, v56, v39
	v_cndmask_b32_e64 v39, v47, v54, s[42:43]
	s_waitcnt lgkmcnt(0)
	v_fmac_f32_e32 v38, v54, v34
	v_cndmask_b32_e64 v34, v39, v38, s[40:41]
	v_fmac_f32_e32 v35, v49, v34
	v_fmac_f32_e32 v36, v48, v34
	v_fmac_f32_e32 v40, v46, v34
	v_fmac_f32_e32 v37, v41, v34
	v_add_f32_e32 v35, v58, v35
	v_add_f32_e32 v36, v59, v36
	v_add_f32_e32 v38, v60, v40
	v_add_f32_e32 v34, v61, v37
	v_cvt_pk_bf16_f32 v34, v34, s0
	ds_write_b16 v118, v34 offset:720
	v_cvt_pk_bf16_f32 v34, v42, s0
	ds_write_b16 v118, v34 offset:2592
	v_cvt_pk_bf16_f32 v34, v43, s0
	ds_write_b16 v118, v34 offset:2736
	v_cvt_pk_bf16_f32 v34, v44, s0
	ds_write_b16 v118, v34 offset:2880
	v_cvt_pk_bf16_f32 v34, v45, s0
	ds_write_b16 v118, v34 offset:3024
	v_cvt_pk_bf16_f32 v34, v50, s0
	ds_write_b16 v118, v34 offset:4896
	v_cvt_pk_bf16_f32 v34, v51, s0
	ds_write_b16 v118, v34 offset:5040
	v_cvt_pk_bf16_f32 v34, v52, s0
	ds_write_b16 v118, v34 offset:5184
	v_cvt_pk_bf16_f32 v34, v53, s0
	ds_write_b16 v118, v34 offset:5328
	v_cvt_pk_bf16_f32 v34, v68, s0
	v_cvt_pk_bf16_f32 v35, v35, s0
	ds_write_b16 v118, v34 offset:7200
	v_cvt_pk_bf16_f32 v34, v69, s0
	s_add_u32 s4, s4, 64
	ds_write_b16 v118, v35 offset:288
	v_cvt_pk_bf16_f32 v35, v36, s0
	ds_write_b16 v118, v34 offset:7344
	v_cvt_pk_bf16_f32 v34, v127, s0
	s_addc_u32 s5, s5, 0
	ds_write_b16 v118, v35 offset:432
	v_cvt_pk_bf16_f32 v35, v38, s0
	ds_write_b16 v118, v34 offset:7488
	v_cvt_pk_bf16_f32 v34, v133, s0
	v_add_u32_e32 v117, 64, v117
	v_add_u32_e32 v116, 0x900, v116
	s_cmpk_lg_i32 s4, 0x100
	v_add_u32_e32 v0, 32, v0
	ds_write_b16 v118, v35 offset:576
	ds_write_b16 v118, v34 offset:7632
	s_cbranch_scc1 .LBB0_621
	s_add_i32 s4, s9, s8
	v_or_b32_e32 v0, s4, v71
	s_movk_i32 s13, 0x2c00
	s_waitcnt lgkmcnt(0)
	v_or_b32_e32 v48, s4, v71
	v_mad_i64_i32 v[16:17], s[8:9], v48, s13, v[74:75]
	global_load_dwordx4 v[16:19], v[16:17], off offset:3072
	v_or_b32_e32 v48, s4, v79
	v_mad_i64_i32 v[20:21], s[8:9], v48, s13, v[74:75]
	global_load_dwordx4 v[20:23], v[20:21], off offset:3072
	v_or_b32_e32 v48, s4, v81
	v_mad_i64_i32 v[24:25], s[8:9], v48, s13, v[74:75]
	global_load_dwordx4 v[24:27], v[24:25], off offset:3072
	v_or_b32_e32 v48, s4, v83
	v_mad_i64_i32 v[28:29], s[8:9], v48, s13, v[74:75]
	global_load_dwordx4 v[28:31], v[28:29], off offset:3072
	v_or_b32_e32 v48, s4, v85
	v_mad_i64_i32 v[32:33], s[8:9], v48, s13, v[74:75]
	global_load_dwordx4 v[32:35], v[32:33], off offset:3072
	v_or_b32_e32 v48, s4, v87
	v_mad_i64_i32 v[36:37], s[8:9], v48, s13, v[74:75]
	global_load_dwordx4 v[36:39], v[36:37], off offset:3072
	v_or_b32_e32 v48, s4, v89
	v_mad_i64_i32 v[40:41], s[8:9], v48, s13, v[74:75]
	global_load_dwordx4 v[40:43], v[40:41], off offset:3072
	v_or_b32_e32 v48, s4, v91
	v_mad_i64_i32 v[44:45], s[8:9], v48, s13, v[74:75]
	global_load_dwordx4 v[44:47], v[44:45], off offset:3072
	s_add_i32 s11, s11, s30
	s_cmp_lt_i32 s11, s10
	s_mov_b32 s34, 0x3d372713
	s_mov_b32 s36, 0x3f4c422a
	s_mov_b32 s58, 0xbfb8aa3b
	ds_read_b128 v[2:5], v108 offset:288
	v_mad_i64_i32 v[6:7], s[8:9], v0, s13, v[72:73]
	s_waitcnt lgkmcnt(0)
	s_waitcnt vmcnt(7)
	v_lshlrev_b32_e32 v48, 16, v16
	v_and_b32_e32 v49, 0xffff0000, v16
	v_lshlrev_b32_e32 v50, 16, v17
	v_and_b32_e32 v51, 0xffff0000, v17
	v_lshlrev_b32_e32 v52, 16, v2
	v_and_b32_e32 v53, 0xffff0000, v2
	v_lshlrev_b32_e32 v54, 16, v3
	v_and_b32_e32 v55, 0xffff0000, v3
	v_pk_mul_f32 v[56:57], v[48:49], s[34:35] op_sel_hi:[1,0]
	v_pk_mul_f32 v[58:59], v[50:51], s[34:35] op_sel_hi:[1,0]
	v_pk_mul_f32 v[56:57], v[56:57], v[48:49]
	v_pk_mul_f32 v[58:59], v[58:59], v[50:51]
	v_pk_fma_f32 v[56:57], v[56:57], v[48:49], v[48:49]
	v_pk_fma_f32 v[58:59], v[58:59], v[50:51], v[50:51]
	v_pk_mul_f32 v[56:57], v[56:57], s[36:37] op_sel_hi:[1,0]
	v_pk_mul_f32 v[58:59], v[58:59], s[36:37] op_sel_hi:[1,0]
	v_pk_add_f32 v[56:57], v[56:57], v[56:57]
	v_pk_add_f32 v[58:59], v[58:59], v[58:59]
	v_pk_mul_f32 v[56:57], v[56:57], s[58:59] op_sel_hi:[1,0]
	v_pk_mul_f32 v[58:59], v[58:59], s[58:59] op_sel_hi:[1,0]
	v_exp_f32_e32 v56, v56
	v_exp_f32_e32 v57, v57
	v_exp_f32_e32 v58, v58
	v_exp_f32_e32 v59, v59
	v_pk_add_f32 v[56:57], v[56:57], 1.0 op_sel_hi:[1,0]
	v_pk_add_f32 v[58:59], v[58:59], 1.0 op_sel_hi:[1,0]
	v_rcp_f32_e32 v56, v56
	v_rcp_f32_e32 v57, v57
	v_rcp_f32_e32 v58, v58
	v_rcp_f32_e32 v59, v59
	v_pk_mul_f32 v[56:57], v[56:57], v[48:49]
	v_pk_mul_f32 v[58:59], v[58:59], v[50:51]
	v_pk_mul_f32 v[56:57], v[56:57], v[52:53]
	v_pk_mul_f32 v[58:59], v[58:59], v[54:55]
	v_cvt_pk_bf16_f32 v10, v56, v57
	v_cvt_pk_bf16_f32 v11, v58, v59
	v_lshlrev_b32_e32 v48, 16, v18
	v_and_b32_e32 v49, 0xffff0000, v18
	v_lshlrev_b32_e32 v50, 16, v19
	v_and_b32_e32 v51, 0xffff0000, v19
	v_lshlrev_b32_e32 v52, 16, v4
	v_and_b32_e32 v53, 0xffff0000, v4
	v_lshlrev_b32_e32 v54, 16, v5
	v_and_b32_e32 v55, 0xffff0000, v5
	v_pk_mul_f32 v[56:57], v[48:49], s[34:35] op_sel_hi:[1,0]
	v_pk_mul_f32 v[58:59], v[50:51], s[34:35] op_sel_hi:[1,0]
	v_pk_mul_f32 v[56:57], v[56:57], v[48:49]
	v_pk_mul_f32 v[58:59], v[58:59], v[50:51]
	v_pk_fma_f32 v[56:57], v[56:57], v[48:49], v[48:49]
	v_pk_fma_f32 v[58:59], v[58:59], v[50:51], v[50:51]
	v_pk_mul_f32 v[56:57], v[56:57], s[36:37] op_sel_hi:[1,0]
	v_pk_mul_f32 v[58:59], v[58:59], s[36:37] op_sel_hi:[1,0]
	v_pk_add_f32 v[56:57], v[56:57], v[56:57]
	v_pk_add_f32 v[58:59], v[58:59], v[58:59]
	v_pk_mul_f32 v[56:57], v[56:57], s[58:59] op_sel_hi:[1,0]
	v_pk_mul_f32 v[58:59], v[58:59], s[58:59] op_sel_hi:[1,0]
	v_exp_f32_e32 v56, v56
	v_exp_f32_e32 v57, v57
	v_exp_f32_e32 v58, v58
	v_exp_f32_e32 v59, v59
	v_pk_add_f32 v[56:57], v[56:57], 1.0 op_sel_hi:[1,0]
	v_pk_add_f32 v[58:59], v[58:59], 1.0 op_sel_hi:[1,0]
	v_rcp_f32_e32 v56, v56
	v_rcp_f32_e32 v57, v57
	v_rcp_f32_e32 v58, v58
	v_rcp_f32_e32 v59, v59
	v_pk_mul_f32 v[56:57], v[56:57], v[48:49]
	v_pk_mul_f32 v[58:59], v[58:59], v[50:51]
	v_pk_mul_f32 v[56:57], v[56:57], v[52:53]
	v_pk_mul_f32 v[58:59], v[58:59], v[54:55]
	v_cvt_pk_bf16_f32 v12, v56, v57
	v_cvt_pk_bf16_f32 v13, v58, v59
	global_store_dwordx4 v[6:7], v[10:13], off
	ds_read_b128 v[2:5], v109 offset:288
	v_or_b32_e32 v0, s4, v79
	v_mad_i64_i32 v[6:7], s[8:9], v0, s13, v[72:73]
	s_waitcnt lgkmcnt(0)
	s_waitcnt vmcnt(7)
	v_lshlrev_b32_e32 v48, 16, v20
	v_and_b32_e32 v49, 0xffff0000, v20
	v_lshlrev_b32_e32 v50, 16, v21
	v_and_b32_e32 v51, 0xffff0000, v21
	v_lshlrev_b32_e32 v52, 16, v2
	v_and_b32_e32 v53, 0xffff0000, v2
	v_lshlrev_b32_e32 v54, 16, v3
	v_and_b32_e32 v55, 0xffff0000, v3
	v_pk_mul_f32 v[56:57], v[48:49], s[34:35] op_sel_hi:[1,0]
	v_pk_mul_f32 v[58:59], v[50:51], s[34:35] op_sel_hi:[1,0]
	v_pk_mul_f32 v[56:57], v[56:57], v[48:49]
	v_pk_mul_f32 v[58:59], v[58:59], v[50:51]
	v_pk_fma_f32 v[56:57], v[56:57], v[48:49], v[48:49]
	v_pk_fma_f32 v[58:59], v[58:59], v[50:51], v[50:51]
	v_pk_mul_f32 v[56:57], v[56:57], s[36:37] op_sel_hi:[1,0]
	v_pk_mul_f32 v[58:59], v[58:59], s[36:37] op_sel_hi:[1,0]
	v_pk_add_f32 v[56:57], v[56:57], v[56:57]
	v_pk_add_f32 v[58:59], v[58:59], v[58:59]
	v_pk_mul_f32 v[56:57], v[56:57], s[58:59] op_sel_hi:[1,0]
	v_pk_mul_f32 v[58:59], v[58:59], s[58:59] op_sel_hi:[1,0]
	v_exp_f32_e32 v56, v56
	v_exp_f32_e32 v57, v57
	v_exp_f32_e32 v58, v58
	v_exp_f32_e32 v59, v59
	v_pk_add_f32 v[56:57], v[56:57], 1.0 op_sel_hi:[1,0]
	v_pk_add_f32 v[58:59], v[58:59], 1.0 op_sel_hi:[1,0]
	v_rcp_f32_e32 v56, v56
	v_rcp_f32_e32 v57, v57
	v_rcp_f32_e32 v58, v58
	v_rcp_f32_e32 v59, v59
	v_pk_mul_f32 v[56:57], v[56:57], v[48:49]
	v_pk_mul_f32 v[58:59], v[58:59], v[50:51]
	v_pk_mul_f32 v[56:57], v[56:57], v[52:53]
	v_pk_mul_f32 v[58:59], v[58:59], v[54:55]
	v_cvt_pk_bf16_f32 v10, v56, v57
	v_cvt_pk_bf16_f32 v11, v58, v59
	v_lshlrev_b32_e32 v48, 16, v22
	v_and_b32_e32 v49, 0xffff0000, v22
	v_lshlrev_b32_e32 v50, 16, v23
	v_and_b32_e32 v51, 0xffff0000, v23
	v_lshlrev_b32_e32 v52, 16, v4
	v_and_b32_e32 v53, 0xffff0000, v4
	v_lshlrev_b32_e32 v54, 16, v5
	v_and_b32_e32 v55, 0xffff0000, v5
	v_pk_mul_f32 v[56:57], v[48:49], s[34:35] op_sel_hi:[1,0]
	v_pk_mul_f32 v[58:59], v[50:51], s[34:35] op_sel_hi:[1,0]
	v_pk_mul_f32 v[56:57], v[56:57], v[48:49]
	v_pk_mul_f32 v[58:59], v[58:59], v[50:51]
	v_pk_fma_f32 v[56:57], v[56:57], v[48:49], v[48:49]
	v_pk_fma_f32 v[58:59], v[58:59], v[50:51], v[50:51]
	v_pk_mul_f32 v[56:57], v[56:57], s[36:37] op_sel_hi:[1,0]
	v_pk_mul_f32 v[58:59], v[58:59], s[36:37] op_sel_hi:[1,0]
	v_pk_add_f32 v[56:57], v[56:57], v[56:57]
	v_pk_add_f32 v[58:59], v[58:59], v[58:59]
	v_pk_mul_f32 v[56:57], v[56:57], s[58:59] op_sel_hi:[1,0]
	v_pk_mul_f32 v[58:59], v[58:59], s[58:59] op_sel_hi:[1,0]
	v_exp_f32_e32 v56, v56
	v_exp_f32_e32 v57, v57
	v_exp_f32_e32 v58, v58
	v_exp_f32_e32 v59, v59
	v_pk_add_f32 v[56:57], v[56:57], 1.0 op_sel_hi:[1,0]
	v_pk_add_f32 v[58:59], v[58:59], 1.0 op_sel_hi:[1,0]
	v_rcp_f32_e32 v56, v56
	v_rcp_f32_e32 v57, v57
	v_rcp_f32_e32 v58, v58
	v_rcp_f32_e32 v59, v59
	v_pk_mul_f32 v[56:57], v[56:57], v[48:49]
	v_pk_mul_f32 v[58:59], v[58:59], v[50:51]
	v_pk_mul_f32 v[56:57], v[56:57], v[52:53]
	v_pk_mul_f32 v[58:59], v[58:59], v[54:55]
	v_cvt_pk_bf16_f32 v12, v56, v57
	v_cvt_pk_bf16_f32 v13, v58, v59
	global_store_dwordx4 v[6:7], v[10:13], off
	ds_read_b128 v[2:5], v110 offset:288
	v_or_b32_e32 v0, s4, v81
	v_mad_i64_i32 v[6:7], s[8:9], v0, s13, v[72:73]
	s_waitcnt lgkmcnt(0)
	s_waitcnt vmcnt(7)
	v_lshlrev_b32_e32 v48, 16, v24
	v_and_b32_e32 v49, 0xffff0000, v24
	v_lshlrev_b32_e32 v50, 16, v25
	v_and_b32_e32 v51, 0xffff0000, v25
	v_lshlrev_b32_e32 v52, 16, v2
	v_and_b32_e32 v53, 0xffff0000, v2
	v_lshlrev_b32_e32 v54, 16, v3
	v_and_b32_e32 v55, 0xffff0000, v3
	v_pk_mul_f32 v[56:57], v[48:49], s[34:35] op_sel_hi:[1,0]
	v_pk_mul_f32 v[58:59], v[50:51], s[34:35] op_sel_hi:[1,0]
	v_pk_mul_f32 v[56:57], v[56:57], v[48:49]
	v_pk_mul_f32 v[58:59], v[58:59], v[50:51]
	v_pk_fma_f32 v[56:57], v[56:57], v[48:49], v[48:49]
	v_pk_fma_f32 v[58:59], v[58:59], v[50:51], v[50:51]
	v_pk_mul_f32 v[56:57], v[56:57], s[36:37] op_sel_hi:[1,0]
	v_pk_mul_f32 v[58:59], v[58:59], s[36:37] op_sel_hi:[1,0]
	v_pk_add_f32 v[56:57], v[56:57], v[56:57]
	v_pk_add_f32 v[58:59], v[58:59], v[58:59]
	v_pk_mul_f32 v[56:57], v[56:57], s[58:59] op_sel_hi:[1,0]
	v_pk_mul_f32 v[58:59], v[58:59], s[58:59] op_sel_hi:[1,0]
	v_exp_f32_e32 v56, v56
	v_exp_f32_e32 v57, v57
	v_exp_f32_e32 v58, v58
	v_exp_f32_e32 v59, v59
	v_pk_add_f32 v[56:57], v[56:57], 1.0 op_sel_hi:[1,0]
	v_pk_add_f32 v[58:59], v[58:59], 1.0 op_sel_hi:[1,0]
	v_rcp_f32_e32 v56, v56
	v_rcp_f32_e32 v57, v57
	v_rcp_f32_e32 v58, v58
	v_rcp_f32_e32 v59, v59
	v_pk_mul_f32 v[56:57], v[56:57], v[48:49]
	v_pk_mul_f32 v[58:59], v[58:59], v[50:51]
	v_pk_mul_f32 v[56:57], v[56:57], v[52:53]
	v_pk_mul_f32 v[58:59], v[58:59], v[54:55]
	v_cvt_pk_bf16_f32 v10, v56, v57
	v_cvt_pk_bf16_f32 v11, v58, v59
	v_lshlrev_b32_e32 v48, 16, v26
	v_and_b32_e32 v49, 0xffff0000, v26
	v_lshlrev_b32_e32 v50, 16, v27
	v_and_b32_e32 v51, 0xffff0000, v27
	v_lshlrev_b32_e32 v52, 16, v4
	v_and_b32_e32 v53, 0xffff0000, v4
	v_lshlrev_b32_e32 v54, 16, v5
	v_and_b32_e32 v55, 0xffff0000, v5
	v_pk_mul_f32 v[56:57], v[48:49], s[34:35] op_sel_hi:[1,0]
	v_pk_mul_f32 v[58:59], v[50:51], s[34:35] op_sel_hi:[1,0]
	v_pk_mul_f32 v[56:57], v[56:57], v[48:49]
	v_pk_mul_f32 v[58:59], v[58:59], v[50:51]
	v_pk_fma_f32 v[56:57], v[56:57], v[48:49], v[48:49]
	v_pk_fma_f32 v[58:59], v[58:59], v[50:51], v[50:51]
	v_pk_mul_f32 v[56:57], v[56:57], s[36:37] op_sel_hi:[1,0]
	v_pk_mul_f32 v[58:59], v[58:59], s[36:37] op_sel_hi:[1,0]
	v_pk_add_f32 v[56:57], v[56:57], v[56:57]
	v_pk_add_f32 v[58:59], v[58:59], v[58:59]
	v_pk_mul_f32 v[56:57], v[56:57], s[58:59] op_sel_hi:[1,0]
	v_pk_mul_f32 v[58:59], v[58:59], s[58:59] op_sel_hi:[1,0]
	v_exp_f32_e32 v56, v56
	v_exp_f32_e32 v57, v57
	v_exp_f32_e32 v58, v58
	v_exp_f32_e32 v59, v59
	v_pk_add_f32 v[56:57], v[56:57], 1.0 op_sel_hi:[1,0]
	v_pk_add_f32 v[58:59], v[58:59], 1.0 op_sel_hi:[1,0]
	v_rcp_f32_e32 v56, v56
	v_rcp_f32_e32 v57, v57
	v_rcp_f32_e32 v58, v58
	v_rcp_f32_e32 v59, v59
	v_pk_mul_f32 v[56:57], v[56:57], v[48:49]
	v_pk_mul_f32 v[58:59], v[58:59], v[50:51]
	v_pk_mul_f32 v[56:57], v[56:57], v[52:53]
	v_pk_mul_f32 v[58:59], v[58:59], v[54:55]
	v_cvt_pk_bf16_f32 v12, v56, v57
	v_cvt_pk_bf16_f32 v13, v58, v59
	global_store_dwordx4 v[6:7], v[10:13], off
	ds_read_b128 v[2:5], v111 offset:288
	v_or_b32_e32 v0, s4, v83
	v_mad_i64_i32 v[6:7], s[8:9], v0, s13, v[72:73]
	s_waitcnt lgkmcnt(0)
	s_waitcnt vmcnt(7)
	v_lshlrev_b32_e32 v48, 16, v28
	v_and_b32_e32 v49, 0xffff0000, v28
	v_lshlrev_b32_e32 v50, 16, v29
	v_and_b32_e32 v51, 0xffff0000, v29
	v_lshlrev_b32_e32 v52, 16, v2
	v_and_b32_e32 v53, 0xffff0000, v2
	v_lshlrev_b32_e32 v54, 16, v3
	v_and_b32_e32 v55, 0xffff0000, v3
	v_pk_mul_f32 v[56:57], v[48:49], s[34:35] op_sel_hi:[1,0]
	v_pk_mul_f32 v[58:59], v[50:51], s[34:35] op_sel_hi:[1,0]
	v_pk_mul_f32 v[56:57], v[56:57], v[48:49]
	v_pk_mul_f32 v[58:59], v[58:59], v[50:51]
	v_pk_fma_f32 v[56:57], v[56:57], v[48:49], v[48:49]
	v_pk_fma_f32 v[58:59], v[58:59], v[50:51], v[50:51]
	v_pk_mul_f32 v[56:57], v[56:57], s[36:37] op_sel_hi:[1,0]
	v_pk_mul_f32 v[58:59], v[58:59], s[36:37] op_sel_hi:[1,0]
	v_pk_add_f32 v[56:57], v[56:57], v[56:57]
	v_pk_add_f32 v[58:59], v[58:59], v[58:59]
	v_pk_mul_f32 v[56:57], v[56:57], s[58:59] op_sel_hi:[1,0]
	v_pk_mul_f32 v[58:59], v[58:59], s[58:59] op_sel_hi:[1,0]
	v_exp_f32_e32 v56, v56
	v_exp_f32_e32 v57, v57
	v_exp_f32_e32 v58, v58
	v_exp_f32_e32 v59, v59
	v_pk_add_f32 v[56:57], v[56:57], 1.0 op_sel_hi:[1,0]
	v_pk_add_f32 v[58:59], v[58:59], 1.0 op_sel_hi:[1,0]
	v_rcp_f32_e32 v56, v56
	v_rcp_f32_e32 v57, v57
	v_rcp_f32_e32 v58, v58
	v_rcp_f32_e32 v59, v59
	v_pk_mul_f32 v[56:57], v[56:57], v[48:49]
	v_pk_mul_f32 v[58:59], v[58:59], v[50:51]
	v_pk_mul_f32 v[56:57], v[56:57], v[52:53]
	v_pk_mul_f32 v[58:59], v[58:59], v[54:55]
	v_cvt_pk_bf16_f32 v10, v56, v57
	v_cvt_pk_bf16_f32 v11, v58, v59
	v_lshlrev_b32_e32 v48, 16, v30
	v_and_b32_e32 v49, 0xffff0000, v30
	v_lshlrev_b32_e32 v50, 16, v31
	v_and_b32_e32 v51, 0xffff0000, v31
	v_lshlrev_b32_e32 v52, 16, v4
	v_and_b32_e32 v53, 0xffff0000, v4
	v_lshlrev_b32_e32 v54, 16, v5
	v_and_b32_e32 v55, 0xffff0000, v5
	v_pk_mul_f32 v[56:57], v[48:49], s[34:35] op_sel_hi:[1,0]
	v_pk_mul_f32 v[58:59], v[50:51], s[34:35] op_sel_hi:[1,0]
	v_pk_mul_f32 v[56:57], v[56:57], v[48:49]
	v_pk_mul_f32 v[58:59], v[58:59], v[50:51]
	v_pk_fma_f32 v[56:57], v[56:57], v[48:49], v[48:49]
	v_pk_fma_f32 v[58:59], v[58:59], v[50:51], v[50:51]
	v_pk_mul_f32 v[56:57], v[56:57], s[36:37] op_sel_hi:[1,0]
	v_pk_mul_f32 v[58:59], v[58:59], s[36:37] op_sel_hi:[1,0]
	v_pk_add_f32 v[56:57], v[56:57], v[56:57]
	v_pk_add_f32 v[58:59], v[58:59], v[58:59]
	v_pk_mul_f32 v[56:57], v[56:57], s[58:59] op_sel_hi:[1,0]
	v_pk_mul_f32 v[58:59], v[58:59], s[58:59] op_sel_hi:[1,0]
	v_exp_f32_e32 v56, v56
	v_exp_f32_e32 v57, v57
	v_exp_f32_e32 v58, v58
	v_exp_f32_e32 v59, v59
	v_pk_add_f32 v[56:57], v[56:57], 1.0 op_sel_hi:[1,0]
	v_pk_add_f32 v[58:59], v[58:59], 1.0 op_sel_hi:[1,0]
	v_rcp_f32_e32 v56, v56
	v_rcp_f32_e32 v57, v57
	v_rcp_f32_e32 v58, v58
	v_rcp_f32_e32 v59, v59
	v_pk_mul_f32 v[56:57], v[56:57], v[48:49]
	v_pk_mul_f32 v[58:59], v[58:59], v[50:51]
	v_pk_mul_f32 v[56:57], v[56:57], v[52:53]
	v_pk_mul_f32 v[58:59], v[58:59], v[54:55]
	v_cvt_pk_bf16_f32 v12, v56, v57
	v_cvt_pk_bf16_f32 v13, v58, v59
	global_store_dwordx4 v[6:7], v[10:13], off
	ds_read_b128 v[2:5], v112 offset:288
	v_or_b32_e32 v0, s4, v85
	v_mad_i64_i32 v[6:7], s[8:9], v0, s13, v[72:73]
	s_waitcnt lgkmcnt(0)
	s_waitcnt vmcnt(7)
	v_lshlrev_b32_e32 v48, 16, v32
	v_and_b32_e32 v49, 0xffff0000, v32
	v_lshlrev_b32_e32 v50, 16, v33
	v_and_b32_e32 v51, 0xffff0000, v33
	v_lshlrev_b32_e32 v52, 16, v2
	v_and_b32_e32 v53, 0xffff0000, v2
	v_lshlrev_b32_e32 v54, 16, v3
	v_and_b32_e32 v55, 0xffff0000, v3
	v_pk_mul_f32 v[56:57], v[48:49], s[34:35] op_sel_hi:[1,0]
	v_pk_mul_f32 v[58:59], v[50:51], s[34:35] op_sel_hi:[1,0]
	v_pk_mul_f32 v[56:57], v[56:57], v[48:49]
	v_pk_mul_f32 v[58:59], v[58:59], v[50:51]
	v_pk_fma_f32 v[56:57], v[56:57], v[48:49], v[48:49]
	v_pk_fma_f32 v[58:59], v[58:59], v[50:51], v[50:51]
	v_pk_mul_f32 v[56:57], v[56:57], s[36:37] op_sel_hi:[1,0]
	v_pk_mul_f32 v[58:59], v[58:59], s[36:37] op_sel_hi:[1,0]
	v_pk_add_f32 v[56:57], v[56:57], v[56:57]
	v_pk_add_f32 v[58:59], v[58:59], v[58:59]
	v_pk_mul_f32 v[56:57], v[56:57], s[58:59] op_sel_hi:[1,0]
	v_pk_mul_f32 v[58:59], v[58:59], s[58:59] op_sel_hi:[1,0]
	v_exp_f32_e32 v56, v56
	v_exp_f32_e32 v57, v57
	v_exp_f32_e32 v58, v58
	v_exp_f32_e32 v59, v59
	v_pk_add_f32 v[56:57], v[56:57], 1.0 op_sel_hi:[1,0]
	v_pk_add_f32 v[58:59], v[58:59], 1.0 op_sel_hi:[1,0]
	v_rcp_f32_e32 v56, v56
	v_rcp_f32_e32 v57, v57
	v_rcp_f32_e32 v58, v58
	v_rcp_f32_e32 v59, v59
	v_pk_mul_f32 v[56:57], v[56:57], v[48:49]
	v_pk_mul_f32 v[58:59], v[58:59], v[50:51]
	v_pk_mul_f32 v[56:57], v[56:57], v[52:53]
	v_pk_mul_f32 v[58:59], v[58:59], v[54:55]
	v_cvt_pk_bf16_f32 v10, v56, v57
	v_cvt_pk_bf16_f32 v11, v58, v59
	v_lshlrev_b32_e32 v48, 16, v34
	v_and_b32_e32 v49, 0xffff0000, v34
	v_lshlrev_b32_e32 v50, 16, v35
	v_and_b32_e32 v51, 0xffff0000, v35
	v_lshlrev_b32_e32 v52, 16, v4
	v_and_b32_e32 v53, 0xffff0000, v4
	v_lshlrev_b32_e32 v54, 16, v5
	v_and_b32_e32 v55, 0xffff0000, v5
	v_pk_mul_f32 v[56:57], v[48:49], s[34:35] op_sel_hi:[1,0]
	v_pk_mul_f32 v[58:59], v[50:51], s[34:35] op_sel_hi:[1,0]
	v_pk_mul_f32 v[56:57], v[56:57], v[48:49]
	v_pk_mul_f32 v[58:59], v[58:59], v[50:51]
	v_pk_fma_f32 v[56:57], v[56:57], v[48:49], v[48:49]
	v_pk_fma_f32 v[58:59], v[58:59], v[50:51], v[50:51]
	v_pk_mul_f32 v[56:57], v[56:57], s[36:37] op_sel_hi:[1,0]
	v_pk_mul_f32 v[58:59], v[58:59], s[36:37] op_sel_hi:[1,0]
	v_pk_add_f32 v[56:57], v[56:57], v[56:57]
	v_pk_add_f32 v[58:59], v[58:59], v[58:59]
	v_pk_mul_f32 v[56:57], v[56:57], s[58:59] op_sel_hi:[1,0]
	v_pk_mul_f32 v[58:59], v[58:59], s[58:59] op_sel_hi:[1,0]
	v_exp_f32_e32 v56, v56
	v_exp_f32_e32 v57, v57
	v_exp_f32_e32 v58, v58
	v_exp_f32_e32 v59, v59
	v_pk_add_f32 v[56:57], v[56:57], 1.0 op_sel_hi:[1,0]
	v_pk_add_f32 v[58:59], v[58:59], 1.0 op_sel_hi:[1,0]
	v_rcp_f32_e32 v56, v56
	v_rcp_f32_e32 v57, v57
	v_rcp_f32_e32 v58, v58
	v_rcp_f32_e32 v59, v59
	v_pk_mul_f32 v[56:57], v[56:57], v[48:49]
	v_pk_mul_f32 v[58:59], v[58:59], v[50:51]
	v_pk_mul_f32 v[56:57], v[56:57], v[52:53]
	v_pk_mul_f32 v[58:59], v[58:59], v[54:55]
	v_cvt_pk_bf16_f32 v12, v56, v57
	v_cvt_pk_bf16_f32 v13, v58, v59
	global_store_dwordx4 v[6:7], v[10:13], off
	ds_read_b128 v[2:5], v113 offset:288
	v_or_b32_e32 v0, s4, v87
	v_mad_i64_i32 v[6:7], s[8:9], v0, s13, v[72:73]
	s_waitcnt lgkmcnt(0)
	s_waitcnt vmcnt(7)
	v_lshlrev_b32_e32 v48, 16, v36
	v_and_b32_e32 v49, 0xffff0000, v36
	v_lshlrev_b32_e32 v50, 16, v37
	v_and_b32_e32 v51, 0xffff0000, v37
	v_lshlrev_b32_e32 v52, 16, v2
	v_and_b32_e32 v53, 0xffff0000, v2
	v_lshlrev_b32_e32 v54, 16, v3
	v_and_b32_e32 v55, 0xffff0000, v3
	v_pk_mul_f32 v[56:57], v[48:49], s[34:35] op_sel_hi:[1,0]
	v_pk_mul_f32 v[58:59], v[50:51], s[34:35] op_sel_hi:[1,0]
	v_pk_mul_f32 v[56:57], v[56:57], v[48:49]
	v_pk_mul_f32 v[58:59], v[58:59], v[50:51]
	v_pk_fma_f32 v[56:57], v[56:57], v[48:49], v[48:49]
	v_pk_fma_f32 v[58:59], v[58:59], v[50:51], v[50:51]
	v_pk_mul_f32 v[56:57], v[56:57], s[36:37] op_sel_hi:[1,0]
	v_pk_mul_f32 v[58:59], v[58:59], s[36:37] op_sel_hi:[1,0]
	v_pk_add_f32 v[56:57], v[56:57], v[56:57]
	v_pk_add_f32 v[58:59], v[58:59], v[58:59]
	v_pk_mul_f32 v[56:57], v[56:57], s[58:59] op_sel_hi:[1,0]
	v_pk_mul_f32 v[58:59], v[58:59], s[58:59] op_sel_hi:[1,0]
	v_exp_f32_e32 v56, v56
	v_exp_f32_e32 v57, v57
	v_exp_f32_e32 v58, v58
	v_exp_f32_e32 v59, v59
	v_pk_add_f32 v[56:57], v[56:57], 1.0 op_sel_hi:[1,0]
	v_pk_add_f32 v[58:59], v[58:59], 1.0 op_sel_hi:[1,0]
	v_rcp_f32_e32 v56, v56
	v_rcp_f32_e32 v57, v57
	v_rcp_f32_e32 v58, v58
	v_rcp_f32_e32 v59, v59
	v_pk_mul_f32 v[56:57], v[56:57], v[48:49]
	v_pk_mul_f32 v[58:59], v[58:59], v[50:51]
	v_pk_mul_f32 v[56:57], v[56:57], v[52:53]
	v_pk_mul_f32 v[58:59], v[58:59], v[54:55]
	v_cvt_pk_bf16_f32 v10, v56, v57
	v_cvt_pk_bf16_f32 v11, v58, v59
	v_lshlrev_b32_e32 v48, 16, v38
	v_and_b32_e32 v49, 0xffff0000, v38
	v_lshlrev_b32_e32 v50, 16, v39
	v_and_b32_e32 v51, 0xffff0000, v39
	v_lshlrev_b32_e32 v52, 16, v4
	v_and_b32_e32 v53, 0xffff0000, v4
	v_lshlrev_b32_e32 v54, 16, v5
	v_and_b32_e32 v55, 0xffff0000, v5
	v_pk_mul_f32 v[56:57], v[48:49], s[34:35] op_sel_hi:[1,0]
	v_pk_mul_f32 v[58:59], v[50:51], s[34:35] op_sel_hi:[1,0]
	v_pk_mul_f32 v[56:57], v[56:57], v[48:49]
	v_pk_mul_f32 v[58:59], v[58:59], v[50:51]
	v_pk_fma_f32 v[56:57], v[56:57], v[48:49], v[48:49]
	v_pk_fma_f32 v[58:59], v[58:59], v[50:51], v[50:51]
	v_pk_mul_f32 v[56:57], v[56:57], s[36:37] op_sel_hi:[1,0]
	v_pk_mul_f32 v[58:59], v[58:59], s[36:37] op_sel_hi:[1,0]
	v_pk_add_f32 v[56:57], v[56:57], v[56:57]
	v_pk_add_f32 v[58:59], v[58:59], v[58:59]
	v_pk_mul_f32 v[56:57], v[56:57], s[58:59] op_sel_hi:[1,0]
	v_pk_mul_f32 v[58:59], v[58:59], s[58:59] op_sel_hi:[1,0]
	v_exp_f32_e32 v56, v56
	v_exp_f32_e32 v57, v57
	v_exp_f32_e32 v58, v58
	v_exp_f32_e32 v59, v59
	v_pk_add_f32 v[56:57], v[56:57], 1.0 op_sel_hi:[1,0]
	v_pk_add_f32 v[58:59], v[58:59], 1.0 op_sel_hi:[1,0]
	v_rcp_f32_e32 v56, v56
	v_rcp_f32_e32 v57, v57
	v_rcp_f32_e32 v58, v58
	v_rcp_f32_e32 v59, v59
	v_pk_mul_f32 v[56:57], v[56:57], v[48:49]
	v_pk_mul_f32 v[58:59], v[58:59], v[50:51]
	v_pk_mul_f32 v[56:57], v[56:57], v[52:53]
	v_pk_mul_f32 v[58:59], v[58:59], v[54:55]
	v_cvt_pk_bf16_f32 v12, v56, v57
	v_cvt_pk_bf16_f32 v13, v58, v59
	global_store_dwordx4 v[6:7], v[10:13], off
	ds_read_b128 v[2:5], v114 offset:288
	v_or_b32_e32 v0, s4, v89
	v_mad_i64_i32 v[6:7], s[8:9], v0, s13, v[72:73]
	s_waitcnt lgkmcnt(0)
	s_waitcnt vmcnt(7)
	v_lshlrev_b32_e32 v48, 16, v40
	v_and_b32_e32 v49, 0xffff0000, v40
	v_lshlrev_b32_e32 v50, 16, v41
	v_and_b32_e32 v51, 0xffff0000, v41
	v_lshlrev_b32_e32 v52, 16, v2
	v_and_b32_e32 v53, 0xffff0000, v2
	v_lshlrev_b32_e32 v54, 16, v3
	v_and_b32_e32 v55, 0xffff0000, v3
	v_pk_mul_f32 v[56:57], v[48:49], s[34:35] op_sel_hi:[1,0]
	v_pk_mul_f32 v[58:59], v[50:51], s[34:35] op_sel_hi:[1,0]
	v_pk_mul_f32 v[56:57], v[56:57], v[48:49]
	v_pk_mul_f32 v[58:59], v[58:59], v[50:51]
	v_pk_fma_f32 v[56:57], v[56:57], v[48:49], v[48:49]
	v_pk_fma_f32 v[58:59], v[58:59], v[50:51], v[50:51]
	v_pk_mul_f32 v[56:57], v[56:57], s[36:37] op_sel_hi:[1,0]
	v_pk_mul_f32 v[58:59], v[58:59], s[36:37] op_sel_hi:[1,0]
	v_pk_add_f32 v[56:57], v[56:57], v[56:57]
	v_pk_add_f32 v[58:59], v[58:59], v[58:59]
	v_pk_mul_f32 v[56:57], v[56:57], s[58:59] op_sel_hi:[1,0]
	v_pk_mul_f32 v[58:59], v[58:59], s[58:59] op_sel_hi:[1,0]
	v_exp_f32_e32 v56, v56
	v_exp_f32_e32 v57, v57
	v_exp_f32_e32 v58, v58
	v_exp_f32_e32 v59, v59
	v_pk_add_f32 v[56:57], v[56:57], 1.0 op_sel_hi:[1,0]
	v_pk_add_f32 v[58:59], v[58:59], 1.0 op_sel_hi:[1,0]
	v_rcp_f32_e32 v56, v56
	v_rcp_f32_e32 v57, v57
	v_rcp_f32_e32 v58, v58
	v_rcp_f32_e32 v59, v59
	v_pk_mul_f32 v[56:57], v[56:57], v[48:49]
	v_pk_mul_f32 v[58:59], v[58:59], v[50:51]
	v_pk_mul_f32 v[56:57], v[56:57], v[52:53]
	v_pk_mul_f32 v[58:59], v[58:59], v[54:55]
	v_cvt_pk_bf16_f32 v10, v56, v57
	v_cvt_pk_bf16_f32 v11, v58, v59
	v_lshlrev_b32_e32 v48, 16, v42
	v_and_b32_e32 v49, 0xffff0000, v42
	v_lshlrev_b32_e32 v50, 16, v43
	v_and_b32_e32 v51, 0xffff0000, v43
	v_lshlrev_b32_e32 v52, 16, v4
	v_and_b32_e32 v53, 0xffff0000, v4
	v_lshlrev_b32_e32 v54, 16, v5
	v_and_b32_e32 v55, 0xffff0000, v5
	v_pk_mul_f32 v[56:57], v[48:49], s[34:35] op_sel_hi:[1,0]
	v_pk_mul_f32 v[58:59], v[50:51], s[34:35] op_sel_hi:[1,0]
	v_pk_mul_f32 v[56:57], v[56:57], v[48:49]
	v_pk_mul_f32 v[58:59], v[58:59], v[50:51]
	v_pk_fma_f32 v[56:57], v[56:57], v[48:49], v[48:49]
	v_pk_fma_f32 v[58:59], v[58:59], v[50:51], v[50:51]
	v_pk_mul_f32 v[56:57], v[56:57], s[36:37] op_sel_hi:[1,0]
	v_pk_mul_f32 v[58:59], v[58:59], s[36:37] op_sel_hi:[1,0]
	v_pk_add_f32 v[56:57], v[56:57], v[56:57]
	v_pk_add_f32 v[58:59], v[58:59], v[58:59]
	v_pk_mul_f32 v[56:57], v[56:57], s[58:59] op_sel_hi:[1,0]
	v_pk_mul_f32 v[58:59], v[58:59], s[58:59] op_sel_hi:[1,0]
	v_exp_f32_e32 v56, v56
	v_exp_f32_e32 v57, v57
	v_exp_f32_e32 v58, v58
	v_exp_f32_e32 v59, v59
	v_pk_add_f32 v[56:57], v[56:57], 1.0 op_sel_hi:[1,0]
	v_pk_add_f32 v[58:59], v[58:59], 1.0 op_sel_hi:[1,0]
	v_rcp_f32_e32 v56, v56
	v_rcp_f32_e32 v57, v57
	v_rcp_f32_e32 v58, v58
	v_rcp_f32_e32 v59, v59
	v_pk_mul_f32 v[56:57], v[56:57], v[48:49]
	v_pk_mul_f32 v[58:59], v[58:59], v[50:51]
	v_pk_mul_f32 v[56:57], v[56:57], v[52:53]
	v_pk_mul_f32 v[58:59], v[58:59], v[54:55]
	v_cvt_pk_bf16_f32 v12, v56, v57
	v_cvt_pk_bf16_f32 v13, v58, v59
	global_store_dwordx4 v[6:7], v[10:13], off
	ds_read_b128 v[2:5], v115 offset:288
	v_or_b32_e32 v0, s4, v91
	v_mad_i64_i32 v[6:7], s[8:9], v0, s13, v[72:73]
	s_waitcnt lgkmcnt(0)
	s_waitcnt vmcnt(7)
	v_lshlrev_b32_e32 v48, 16, v44
	v_and_b32_e32 v49, 0xffff0000, v44
	v_lshlrev_b32_e32 v50, 16, v45
	v_and_b32_e32 v51, 0xffff0000, v45
	v_lshlrev_b32_e32 v52, 16, v2
	v_and_b32_e32 v53, 0xffff0000, v2
	v_lshlrev_b32_e32 v54, 16, v3
	v_and_b32_e32 v55, 0xffff0000, v3
	v_pk_mul_f32 v[56:57], v[48:49], s[34:35] op_sel_hi:[1,0]
	v_pk_mul_f32 v[58:59], v[50:51], s[34:35] op_sel_hi:[1,0]
	v_pk_mul_f32 v[56:57], v[56:57], v[48:49]
	v_pk_mul_f32 v[58:59], v[58:59], v[50:51]
	v_pk_fma_f32 v[56:57], v[56:57], v[48:49], v[48:49]
	v_pk_fma_f32 v[58:59], v[58:59], v[50:51], v[50:51]
	v_pk_mul_f32 v[56:57], v[56:57], s[36:37] op_sel_hi:[1,0]
	v_pk_mul_f32 v[58:59], v[58:59], s[36:37] op_sel_hi:[1,0]
	v_pk_add_f32 v[56:57], v[56:57], v[56:57]
	v_pk_add_f32 v[58:59], v[58:59], v[58:59]
	v_pk_mul_f32 v[56:57], v[56:57], s[58:59] op_sel_hi:[1,0]
	v_pk_mul_f32 v[58:59], v[58:59], s[58:59] op_sel_hi:[1,0]
	v_exp_f32_e32 v56, v56
	v_exp_f32_e32 v57, v57
	v_exp_f32_e32 v58, v58
	v_exp_f32_e32 v59, v59
	v_pk_add_f32 v[56:57], v[56:57], 1.0 op_sel_hi:[1,0]
	v_pk_add_f32 v[58:59], v[58:59], 1.0 op_sel_hi:[1,0]
	v_rcp_f32_e32 v56, v56
	v_rcp_f32_e32 v57, v57
	v_rcp_f32_e32 v58, v58
	v_rcp_f32_e32 v59, v59
	v_pk_mul_f32 v[56:57], v[56:57], v[48:49]
	v_pk_mul_f32 v[58:59], v[58:59], v[50:51]
	v_pk_mul_f32 v[56:57], v[56:57], v[52:53]
	v_pk_mul_f32 v[58:59], v[58:59], v[54:55]
	v_cvt_pk_bf16_f32 v10, v56, v57
	v_cvt_pk_bf16_f32 v11, v58, v59
	v_lshlrev_b32_e32 v48, 16, v46
	v_and_b32_e32 v49, 0xffff0000, v46
	v_lshlrev_b32_e32 v50, 16, v47
	v_and_b32_e32 v51, 0xffff0000, v47
	v_lshlrev_b32_e32 v52, 16, v4
	v_and_b32_e32 v53, 0xffff0000, v4
	v_lshlrev_b32_e32 v54, 16, v5
	v_and_b32_e32 v55, 0xffff0000, v5
	v_pk_mul_f32 v[56:57], v[48:49], s[34:35] op_sel_hi:[1,0]
	v_pk_mul_f32 v[58:59], v[50:51], s[34:35] op_sel_hi:[1,0]
	v_pk_mul_f32 v[56:57], v[56:57], v[48:49]
	v_pk_mul_f32 v[58:59], v[58:59], v[50:51]
	v_pk_fma_f32 v[56:57], v[56:57], v[48:49], v[48:49]
	v_pk_fma_f32 v[58:59], v[58:59], v[50:51], v[50:51]
	v_pk_mul_f32 v[56:57], v[56:57], s[36:37] op_sel_hi:[1,0]
	v_pk_mul_f32 v[58:59], v[58:59], s[36:37] op_sel_hi:[1,0]
	v_pk_add_f32 v[56:57], v[56:57], v[56:57]
	v_pk_add_f32 v[58:59], v[58:59], v[58:59]
	v_pk_mul_f32 v[56:57], v[56:57], s[58:59] op_sel_hi:[1,0]
	v_pk_mul_f32 v[58:59], v[58:59], s[58:59] op_sel_hi:[1,0]
	v_exp_f32_e32 v56, v56
	v_exp_f32_e32 v57, v57
	v_exp_f32_e32 v58, v58
	v_exp_f32_e32 v59, v59
	v_pk_add_f32 v[56:57], v[56:57], 1.0 op_sel_hi:[1,0]
	v_pk_add_f32 v[58:59], v[58:59], 1.0 op_sel_hi:[1,0]
	v_rcp_f32_e32 v56, v56
	v_rcp_f32_e32 v57, v57
	v_rcp_f32_e32 v58, v58
	v_rcp_f32_e32 v59, v59
	v_pk_mul_f32 v[56:57], v[56:57], v[48:49]
	v_pk_mul_f32 v[58:59], v[58:59], v[50:51]
	v_pk_mul_f32 v[56:57], v[56:57], v[52:53]
	v_pk_mul_f32 v[58:59], v[58:59], v[54:55]
	v_cvt_pk_bf16_f32 v12, v56, v57
	v_cvt_pk_bf16_f32 v13, v58, v59
	global_store_dwordx4 v[6:7], v[10:13], off
	s_waitcnt lgkmcnt(0)
	s_cbranch_scc1 .LBB0_600
	v_readlane_b32 s44, v253, 43
	v_readlane_b32 s45, v253, 44
	s_movk_i32 s43, 0x4000
	v_readlane_b32 s47, v253, 50
